# baseline (speedup 1.0000x reference)
.LBB2_5:
	ds_read_b128 v[102:105], v120 offset:8192
	ds_read_b128 v[106:109], v120 offset:10240
	ds_read_b128 v[110:113], v120 offset:12288
	v_exp_f32_e32 v69, v46
	v_exp_f32_e32 v71, v47
	v_exp_f32_e32 v73, v48
	v_exp_f32_e32 v75, v49
	ds_read_b128 v[46:49], v120 offset:14336
	v_exp_f32_e32 v42, v42
	v_exp_f32_e32 v43, v43
	v_exp_f32_e32 v44, v44
	v_exp_f32_e32 v45, v45
	v_cvt_pk_f16_f32 v76, v69, v71
	v_cvt_pk_f16_f32 v77, v73, v75
	v_cvt_pk_f16_f32 v78, v42, v43
	v_cvt_pk_f16_f32 v79, v44, v45
	ds_read_b128 v[42:45], v121 offset:8192
	v_exp_f32_e32 v38, v38
	v_exp_f32_e32 v39, v39
	s_waitcnt lgkmcnt(4)
	v_mfma_f32_16x16x32_f16 v[26:29], v[102:105], v[76:79], v[26:29]
	v_exp_f32_e32 v40, v40
	v_exp_f32_e32 v41, v41
	s_waitcnt lgkmcnt(3)
	v_mfma_f32_16x16x32_f16 v[22:25], v[106:109], v[76:79], v[22:25]
	ds_read_b128 v[102:105], v121 offset:10240
	v_exp_f32_e32 v34, v34
	v_exp_f32_e32 v35, v35
	s_waitcnt lgkmcnt(3)
	v_mfma_f32_16x16x32_f16 v[18:21], v[110:113], v[76:79], v[18:21]
	ds_read_b128 v[106:109], v121 offset:12288
	v_exp_f32_e32 v36, v36
	v_exp_f32_e32 v37, v37
	s_waitcnt lgkmcnt(3)
	v_mfma_f32_16x16x32_f16 v[10:13], v[46:49], v[76:79], v[10:13]
	ds_read_b128 v[110:113], v121 offset:14336
	v_mfma_f32_16x16x32_f16 v[14:17], v[116:119], v[76:79], v[14:17]
	v_cvt_pk_f16_f32 v37, v36, v37
	v_cvt_pk_f16_f32 v36, v34, v35
	v_cvt_pk_f16_f32 v35, v40, v41
	v_cvt_pk_f16_f32 v34, v38, v39
	s_mov_b64 s[38:39], 0
	s_waitcnt lgkmcnt(3)
	v_mfma_f32_16x16x32_f16 v[26:29], v[42:45], v[34:37], v[26:29]
	s_waitcnt lgkmcnt(2)
	v_mfma_f32_16x16x32_f16 v[22:25], v[102:105], v[34:37], v[22:25]
	s_waitcnt lgkmcnt(1)
	v_mfma_f32_16x16x32_f16 v[18:21], v[106:109], v[34:37], v[18:21]
	s_waitcnt lgkmcnt(0)
	v_mfma_f32_16x16x32_f16 v[10:13], v[110:113], v[34:37], v[10:13]
	v_mfma_f32_16x16x32_f16 v[14:17], v[116:119], v[34:37], v[14:17]
	s_cmp_eq_u32 s55, 0
	s_cbranch_scc1 .LBB2_6
	s_mov_b32 s80, 0
	s_cmp_eq_u32 s81, 0
	s_cbranch_scc1 .Lattn_A
	s_cmp_eq_u32 s81, 2
	s_cbranch_scc0 .Lattn_post
	s_mov_b32 s81, 0
	s_branch .LBB2_6

.Lattn_A_done:
	s_cmp_eq_u32 s55, 0
	s_cbranch_scc1 .LBB2_5
	s_add_i32 s82, s65, s64
	s_cmp_eq_u32 s82, 0
	s_cbranch_scc1 .Lattn_last_B
	s_mov_b32 s80, 1
	s_branch .LBB2_6
.Lattn_last_B:
	v_mov_b32_e32 v120, v114
	v_mov_b32_e32 v121, v115
	s_mov_b32 s81, 2
	s_branch .LBB2_5
